# speedup vs baseline: 1.0158x; 1.0024x over previous
_Z10ode_kernelPKfPKDF16_S2_PfPKi:
	v_lshrrev_b32_e32 v167, 6, v0
	s_lshr_b32 s3, s2, 3
	v_add_u32_e32 v2, s3, v167
	s_load_dwordx4 s[4:7], s[0:1], 0x0
	s_load_dwordx2 s[12:13], s[0:1], 0x10
	v_and_b32_e32 v130, 3, v2
	v_and_b32_e32 v1, 63, v0
	v_readfirstlane_b32 s3, v130
	v_lshlrev_b32_e32 v166, 4, v1
	s_lshl_b32 s11, s3, 14
	v_lshl_or_b32 v2, v130, 17, v166
	v_mov_b32_e32 v3, 0
	s_and_b32 s17, s11, 0xc000
	s_mov_b32 s9, 0
	s_waitcnt lgkmcnt(0)
	v_lshl_add_u64 v[74:75], s[6:7], 0, v[2:3]
	s_lshl_b32 s8, s17, 1
	v_lshl_add_u64 v[46:47], v[74:75], 0, s[8:9]
	s_movk_i32 s15, 0x1000
	v_add_co_u32_e32 v18, vcc, s15, v46
	s_movk_i32 s14, 0x3000
	s_nop 0
	v_addc_co_u32_e32 v19, vcc, 0, v47, vcc
	v_add_co_u32_e32 v20, vcc, s14, v46
	s_lshl_b32 s10, s2, 10
	s_nop 0
	v_addc_co_u32_e32 v21, vcc, 0, v47, vcc
	s_and_b32 s8, s10, 0x3e000
	s_movk_i32 s16, 0x7000
	v_add_co_u32_e32 v48, vcc, s16, v46
	v_lshl_or_b32 v22, v1, 7, s8
	s_add_i32 s8, s11, 0x4000
	v_addc_co_u32_e32 v49, vcc, 0, v47, vcc
	s_movk_i32 s16, 0x5000
	s_and_b32 s8, s8, 0xc000
	v_add_co_u32_e32 v50, vcc, s16, v46
	s_lshl_b32 s8, s8, 1
	global_load_dwordx4 v[34:37], v[18:19], off offset:2048
	global_load_dwordx4 v[14:17], v[20:21], off offset:2048
	global_load_dwordx4 v[6:9], v[20:21], off offset:1024
	global_load_dwordx4 v[2:5], v[18:19], off offset:1024
	global_load_dwordx4 v[42:45], v[18:19], off offset:3072
	global_load_dwordx4 v[38:41], v[20:21], off offset:3072
	v_addc_co_u32_e32 v51, vcc, 0, v47, vcc
	v_lshl_add_u64 v[72:73], v[74:75], 0, s[8:9]
	v_add_co_u32_e32 v106, vcc, s14, v72
	global_load_dwordx4 v[10:13], v[50:51], off offset:1024
	global_load_dwordx4 v[52:55], v[50:51], off offset:2048
	global_load_dwordx4 v[56:59], v[48:49], off offset:2048
	v_addc_co_u32_e32 v107, vcc, 0, v73, vcc
	v_add_co_u32_e32 v108, vcc, s15, v72
	global_load_dwordx4 v[60:63], v[50:51], off offset:3072
	global_load_dwordx4 v[64:67], v[48:49], off offset:3072
	global_load_ushort v198, v22, s[12:13]
	v_addc_co_u32_e32 v109, vcc, 0, v73, vcc
	global_load_dwordx4 v[68:71], v[108:109], off offset:2048
	global_load_dwordx4 v[78:81], v[106:107], off offset:2048
	global_load_dwordx4 v[82:85], v[106:107], off offset:3072
	global_load_dwordx4 v[86:89], v[108:109], off offset:3072
	s_add_i32 s8, s11, 0x6000
	s_movk_i32 s16, 0x2000
	s_and_b32 s8, s8, 0xe000
	v_add_co_u32_e32 v26, vcc, s16, v46
	s_lshl_b32 s8, s8, 1
	s_nop 0
	v_addc_co_u32_e32 v27, vcc, 0, v47, vcc
	v_lshl_add_u64 v[110:111], v[74:75], 0, s[8:9]
	v_add_co_u32_e32 v112, vcc, s14, v110
	global_load_dwordx4 a[0:3], v[46:47], off
	global_load_dwordx4 a[8:11], v[46:47], off offset:1024
	global_load_dwordx4 a[12:15], v[26:27], off offset:1024
	global_load_dwordx4 a[20:23], v[26:27], off offset:2048
	global_load_dwordx4 a[16:19], v[46:47], off offset:2048
	global_load_dwordx4 a[24:27], v[46:47], off offset:3072
	global_load_dwordx4 a[4:7], v[20:21], off offset:-4096
	global_load_dwordx4 v[22:25], v[20:21], off
	global_load_dwordx4 a[28:31], v[26:27], off offset:3072
	s_nop 0
	global_load_dwordx4 v[18:21], v[18:19], off
	v_addc_co_u32_e32 v113, vcc, 0, v111, vcc
	v_add_co_u32_e32 v114, vcc, s15, v110
	v_lshl_or_b32 v199, v167, 15, v166
	s_nop 0
	v_addc_co_u32_e32 v115, vcc, 0, v111, vcc
	global_load_dwordx4 v[26:29], v[114:115], off offset:1024
	global_load_dwordx4 v[90:93], v[114:115], off offset:2048
	global_load_dwordx4 v[30:33], v[112:113], off offset:1024
	global_load_dwordx4 v[94:97], v[112:113], off offset:2048
	global_load_dwordx4 v[98:101], v[114:115], off offset:3072
	global_load_dwordx4 v[102:105], v[112:113], off offset:3072
	s_movk_i32 s8, 0x6000
	s_load_dwordx2 s[6:7], s[0:1], 0x20
	v_lshlrev_b32_e32 v76, 1, v0
	v_and_b32_e32 v200, 7, v0
	v_and_b32_e32 v128, 64, v76
	v_and_b32_e32 v179, 15, v0
	v_bfe_u32 v201, v0, 4, 1
	v_mov_b32_e32 v196, 0x44444444
	global_load_dwordx4 a[44:47], v[48:49], off offset:-4096
	s_waitcnt vmcnt(31)
	ds_write_b128 v199, v[14:17] offset:1024
	v_add_co_u32_e32 v14, vcc, s8, v46
	s_movk_i32 s8, 0x4000
	s_nop 0
	v_addc_co_u32_e32 v15, vcc, 0, v47, vcc
	s_waitcnt vmcnt(28)
	ds_write_b128 v199, v[42:45] offset:2048
	v_add_co_u32_e32 v42, vcc, s8, v46
	ds_write_b128 v199, v[34:37]
	s_nop 0
	v_addc_co_u32_e32 v43, vcc, 0, v47, vcc
	s_waitcnt vmcnt(27)
	ds_write_b128 v199, v[38:41] offset:3072
	v_add_co_u32_e32 v44, vcc, s16, v72
	global_load_dwordx4 a[36:39], v[14:15], off offset:1024
	global_load_dwordx4 a[32:35], v[42:43], off offset:1024
	global_load_dwordx4 a[48:51], v[42:43], off offset:2048
	global_load_dwordx4 a[52:55], v[14:15], off offset:2048
	global_load_dwordx4 a[60:63], v[14:15], off offset:3072
	global_load_dwordx4 a[40:43], v[50:51], off offset:-4096
	global_load_dwordx4 v[34:37], v[50:51], off
	global_load_dwordx4 v[38:41], v[48:49], off
	s_nop 0
	global_load_dwordx4 v[14:17], v[48:49], off offset:1024
	s_waitcnt vmcnt(34)
	ds_write_b128 v199, v[52:55] offset:4096
	s_waitcnt vmcnt(33)
	ds_write_b128 v199, v[56:59] offset:5120
	v_addc_co_u32_e32 v45, vcc, 0, v73, vcc
	s_xor_b32 s8, s17, 0x8000
	global_load_dwordx4 a[68:71], v[106:107], off offset:-4096
	s_waitcnt vmcnt(33)
	ds_write_b128 v199, v[60:63] offset:6144
	s_waitcnt vmcnt(32)
	ds_write_b128 v199, v[64:67] offset:7168
	v_add_co_u32_e32 v58, vcc, s16, v110
	s_lshl_b32 s8, s8, 1
	global_load_dwordx4 a[56:59], v[42:43], off offset:3072
	global_load_dwordx4 a[64:67], v[72:73], off
	global_load_dwordx4 a[72:75], v[72:73], off offset:1024
	global_load_dwordx4 a[80:83], v[72:73], off offset:2048
	global_load_dwordx4 a[84:87], v[44:45], off offset:2048
	global_load_dwordx4 a[92:95], v[44:45], off offset:3072
	global_load_dwordx4 a[76:79], v[44:45], off offset:1024
	global_load_dwordx4 a[88:91], v[72:73], off offset:3072
	global_load_dwordx4 v[46:49], v[106:107], off
	global_load_dwordx4 v[54:57], v[106:107], off offset:1024
	s_nop 0
	global_load_dwordx4 v[42:45], v[108:109], off
	global_load_dwordx4 v[50:53], v[108:109], off offset:1024
	s_waitcnt vmcnt(42)
	ds_write_b128 v199, v[68:71] offset:8192
	s_waitcnt vmcnt(41)
	ds_write_b128 v199, v[78:81] offset:9216
	s_waitcnt vmcnt(39)
	ds_write_b128 v199, v[86:89] offset:10240
	ds_write_b128 v199, v[82:85] offset:11264
	v_addc_co_u32_e32 v59, vcc, 0, v111, vcc
	v_lshl_add_u64 v[78:79], v[74:75], 0, s[8:9]
	v_add_co_u32_e32 v84, vcc, s14, v78
	global_load_dwordx4 a[96:99], v[110:111], off
	global_load_dwordx4 a[104:107], v[110:111], off offset:1024
	global_load_dwordx4 a[108:111], v[58:59], off offset:1024
	global_load_dwordx4 a[116:119], v[58:59], off offset:2048
	global_load_dwordx4 a[112:115], v[110:111], off offset:2048
	global_load_dwordx4 a[120:123], v[110:111], off offset:3072
	global_load_dwordx4 a[100:103], v[112:113], off offset:-4096
	global_load_dwordx4 v[62:65], v[112:113], off
	global_load_dwordx4 a[124:127], v[58:59], off offset:3072
	s_nop 0
	global_load_dwordx4 v[58:61], v[114:115], off
	v_addc_co_u32_e32 v85, vcc, 0, v79, vcc
	v_add_co_u32_e32 v82, vcc, s15, v78
	s_add_i32 s8, s11, 0xa000
	s_nop 0
	v_addc_co_u32_e32 v83, vcc, 0, v79, vcc
	global_load_dwordx4 v[110:113], v[82:83], off offset:2048
	global_load_dwordx4 v[106:109], v[84:85], off offset:2048
	s_waitcnt vmcnt(39)
	ds_write_b128 v199, v[90:93] offset:12288
	s_waitcnt vmcnt(37)
	ds_write_b128 v199, v[94:97] offset:13312
	s_waitcnt vmcnt(36)
	ds_write_b128 v199, v[98:101] offset:14336
	s_waitcnt vmcnt(35)
	ds_write_b128 v199, v[102:105] offset:15360
	global_load_dwordx4 a[128:131], v[78:79], off
	global_load_dwordx4 a[132:135], v[84:85], off offset:-4096
	global_load_dwordx4 a[136:139], v[78:79], off offset:1024
	global_load_dwordx4 a[144:147], v[78:79], off offset:2048
	global_load_dwordx4 v[102:105], v[82:83], off offset:3072
	global_load_dwordx4 v[98:101], v[84:85], off offset:3072
	s_and_b32 s8, s8, 0xe000
	v_add_co_u32_e32 v80, vcc, s16, v78
	s_lshl_b32 s8, s8, 1
	s_nop 0
	v_addc_co_u32_e32 v81, vcc, 0, v79, vcc
	v_lshl_add_u64 v[122:123], v[74:75], 0, s[8:9]
	v_add_co_u32_e32 v124, vcc, s14, v122
	s_add_i32 s8, s11, 0xc000
	s_nop 0
	v_addc_co_u32_e32 v125, vcc, 0, v123, vcc
	v_add_co_u32_e32 v126, vcc, s15, v122
	s_and_b32 s8, s8, 0xc000
	s_nop 0
	v_addc_co_u32_e32 v127, vcc, 0, v123, vcc
	global_load_dwordx4 v[70:73], v[124:125], off offset:1024
	global_load_dwordx4 v[114:117], v[124:125], off offset:2048
	global_load_dwordx4 v[66:69], v[126:127], off offset:1024
	global_load_dwordx4 v[118:121], v[126:127], off offset:2048
	global_load_dwordx4 a[148:151], v[80:81], off offset:2048
	global_load_dwordx4 a[156:159], v[80:81], off offset:3072
	global_load_dwordx4 v[132:135], v[126:127], off offset:3072
	global_load_dwordx4 v[136:139], v[124:125], off offset:3072
	global_load_dwordx4 a[140:143], v[80:81], off offset:1024
	global_load_dwordx4 a[152:155], v[78:79], off offset:3072
	s_nop 0
	global_load_dwordx4 v[78:81], v[84:85], off
	global_load_dwordx4 v[86:89], v[84:85], off offset:1024
	s_lshl_b32 s8, s8, 1
	v_lshl_add_u64 v[164:165], v[74:75], 0, s[8:9]
	v_add_co_u32_e32 v176, vcc, s14, v164
	s_add_i32 s11, s11, 0xe000
	s_nop 0
	v_addc_co_u32_e32 v177, vcc, 0, v165, vcc
	v_add_co_u32_e32 v184, vcc, s15, v164
	s_and_b32 s8, s11, 0xe000
	s_nop 0
	v_addc_co_u32_e32 v185, vcc, 0, v165, vcc
	global_load_dwordx4 v[140:143], v[184:185], off offset:2048
	global_load_dwordx4 v[144:147], v[176:177], off offset:2048
	global_load_dwordx4 v[148:151], v[176:177], off offset:3072
	global_load_dwordx4 v[152:155], v[184:185], off offset:3072
	s_lshl_b32 s8, s8, 1
	v_lshl_add_u64 v[186:187], v[74:75], 0, s[8:9]
	v_add_co_u32_e32 v188, vcc, s14, v186
	v_and_or_b32 v74, v76, 16, v200
	s_nop 0
	v_addc_co_u32_e32 v189, vcc, 0, v187, vcc
	v_add_co_u32_e32 v190, vcc, s15, v186
	v_lshlrev_b32_e32 v129, 2, v74
	s_nop 0
	v_addc_co_u32_e32 v191, vcc, 0, v187, vcc
	global_load_dwordx4 v[94:97], v[188:189], off offset:1024
	global_load_dwordx4 v[156:159], v[188:189], off offset:2048
	global_load_dwordx4 v[90:93], v[190:191], off offset:1024
	global_load_dwordx4 v[160:163], v[190:191], off offset:2048
	global_load_dwordx4 v[172:175], v[188:189], off offset:3072
	global_load_dwordx4 v[180:183], v[190:191], off offset:3072
	s_waitcnt lgkmcnt(0)
	global_load_dword v131, v129, s[6:7]
	global_load_dwordx4 v[74:77], v[82:83], off
	s_nop 0
	global_load_dwordx4 v[82:85], v[82:83], off offset:1024
	s_waitcnt vmcnt(32)
	ds_write_b128 v199, v[110:113] offset:16384
	s_waitcnt vmcnt(31)
	ds_write_b128 v199, v[106:109] offset:17408
	v_lshlrev_b32_e32 v106, 7, v130
	v_or3_b32 v202, v106, v128, v179
	v_lshlrev_b32_e32 v106, 9, v201
	v_or_b32_e32 v107, 32, v129
	v_or3_b32 v106, v106, s10, v202
	global_load_dword v178, v129, s[6:7] offset:128
	global_load_dword v192, v107, s[6:7] offset:128
	global_load_dword v193, v129, s[6:7] offset:32
	v_ashrrev_i32_e32 v107, 31, v106
	v_lshl_add_u64 v[128:129], v[106:107], 2, s[4:5]
	global_load_dword v171, v[128:129], off
	s_waitcnt vmcnt(30)
	ds_write_b128 v199, v[102:105] offset:18432
	s_waitcnt vmcnt(29)
	ds_write_b128 v199, v[98:101] offset:19456
	v_add_co_u32_e32 v98, vcc, s16, v122
	s_mov_b32 s14, 0x45000000
	s_nop 0
	v_addc_co_u32_e32 v99, vcc, 0, v123, vcc
	global_load_dwordx4 a[160:163], v[122:123], off
	global_load_dwordx4 a[168:171], v[122:123], off offset:1024
	global_load_dwordx4 a[172:175], v[98:99], off offset:1024
	global_load_dwordx4 a[180:183], v[98:99], off offset:2048
	global_load_dwordx4 a[176:179], v[122:123], off offset:2048
	global_load_dwordx4 a[184:187], v[122:123], off offset:3072
	global_load_dword v170, v[128:129], off offset:64
	global_load_dwordx4 a[164:167], v[124:125], off offset:-4096
	global_load_dwordx4 v[102:105], v[124:125], off
	global_load_dwordx4 a[188:191], v[98:99], off offset:3072
	s_nop 0
	global_load_dwordx4 v[98:101], v[126:127], off
	s_waitcnt vmcnt(36)
	ds_write_b128 v199, v[118:121] offset:20480
	ds_write_b128 v199, v[114:117] offset:21504
	global_load_dword v169, v[128:129], off offset:128
	v_add_co_u32_e32 v106, vcc, s16, v164
	s_waitcnt vmcnt(34)
	ds_write_b128 v199, v[132:135] offset:22528
	s_waitcnt vmcnt(33)
	ds_write_b128 v199, v[136:139] offset:23552
	v_addc_co_u32_e32 v107, vcc, 0, v165, vcc
	global_load_dwordx4 a[192:195], v[164:165], off
	global_load_dwordx4 a[196:199], v[176:177], off offset:-4096
	global_load_dwordx4 a[200:203], v[164:165], off offset:1024
	global_load_dwordx4 a[208:211], v[164:165], off offset:2048
	global_load_dwordx4 a[212:215], v[106:107], off offset:2048
	global_load_dwordx4 a[220:223], v[106:107], off offset:3072
	global_load_dwordx4 a[204:207], v[106:107], off offset:1024
	global_load_dwordx4 a[216:219], v[164:165], off offset:3072
	global_load_dwordx4 v[110:113], v[176:177], off
	global_load_dwordx4 v[118:121], v[176:177], off offset:1024
	s_nop 0
	global_load_dwordx4 v[106:109], v[184:185], off
	global_load_dwordx4 v[114:117], v[184:185], off offset:1024
	global_load_dword v168, v[128:129], off offset:192
	v_add_co_u32_e32 v122, vcc, s16, v186
	v_and_b32_e32 v133, 32, v0
	s_nop 0
	v_addc_co_u32_e32 v123, vcc, 0, v187, vcc
	s_waitcnt vmcnt(41)
	ds_write_b128 v199, v[140:143] offset:24576
	s_waitcnt vmcnt(40)
	ds_write_b128 v199, v[144:147] offset:25600
	s_waitcnt vmcnt(38)
	ds_write_b128 v199, v[152:155] offset:26624
	ds_write_b128 v199, v[148:151] offset:27648
	global_load_dwordx4 a[224:227], v[186:187], off
	global_load_dwordx4 a[232:235], v[186:187], off offset:1024
	global_load_dwordx4 a[236:239], v[122:123], off offset:1024
	global_load_dwordx4 a[244:247], v[122:123], off offset:2048
	global_load_dwordx4 a[240:243], v[186:187], off offset:2048
	global_load_dwordx4 a[248:251], v[186:187], off offset:3072
	global_load_dwordx4 a[228:231], v[188:189], off offset:-4096
	global_load_dwordx4 v[126:129], v[188:189], off
	global_load_dwordx4 a[252:255], v[122:123], off offset:3072
	s_nop 0
	global_load_dwordx4 v[122:125], v[190:191], off
	v_lshlrev_b32_e32 v132, 2, v201
	v_lshl_or_b32 v130, v130, 6, v133
	v_lshrrev_b32_e32 v139, 1, v0
	v_and_b32_e32 v203, 24, v139
	s_waitcnt vmcnt(44)
	ds_write_b128 v199, v[160:163] offset:28672
	ds_write_b128 v199, v[156:159] offset:29696
	s_waitcnt vmcnt(42)
	ds_write_b128 v199, v[180:183] offset:30720
	ds_write_b128 v199, v[172:175] offset:31744
	s_waitcnt vmcnt(10) lgkmcnt(0)
	v_lshrrev_b32_e32 v222, 2, v131
	v_and_or_b32 v222, v222, 8, v132
	v_mul_u32_u24_e32 v222, 0x110, v222
	v_and_or_b32 v223, v131, 31, v130
	v_add_lshl_u32 v223, v223, v222, 1
	v_or_b32_e32 v204, 0x20000, v223
	v_lshrrev_b32_e32 v222, 2, v178
	v_and_or_b32 v222, v222, 8, v132
	v_mul_u32_u24_e32 v222, 0x110, v222
	v_and_or_b32 v223, v178, 31, v130
	v_add_lshl_u32 v223, v223, v222, 1
	v_or_b32_e32 v205, 0x20000, v223
	v_lshrrev_b32_e32 v222, 2, v193
	v_and_or_b32 v222, v222, 8, v132
	v_mul_u32_u24_e32 v222, 0x110, v222
	v_and_or_b32 v223, v193, 31, v130
	v_add_lshl_u32 v223, v223, v222, 1
	v_or_b32_e32 v206, 0x20000, v223
	v_lshrrev_b32_e32 v222, 2, v192
	v_and_or_b32 v222, v222, 8, v132
	v_mul_u32_u24_e32 v222, 0x110, v222
	v_and_or_b32 v223, v192, 31, v130
	v_add_lshl_u32 v223, v223, v222, 1
	v_or_b32_e32 v207, 0x20000, v223
	s_movk_i32 s43, 0x110
	v_mad_u32_u24 v224, v179, s43, v203
	v_mov_b32_e32 v225, 0x20000
	v_lshl_or_b32 v224, v224, 1, v225
	s_lshl_b32 s43, s3, 1
	s_add_u32 s52, s43, 0
	s_and_b32 s52, s52, 7
	s_lshl_b32 s52, s52, 6
	s_nop 0
	v_add_u32_e32 v208, s52, v224
	s_add_u32 s52, s43, 1
	s_and_b32 s52, s52, 7
	s_lshl_b32 s52, s52, 6
	s_sub_u32 s52, s52, 64
	s_nop 0
	v_add_u32_e32 v209, s52, v224
	s_add_u32 s52, s43, 2
	s_and_b32 s52, s52, 7
	s_lshl_b32 s52, s52, 6
	s_nop 0
	v_add_u32_e32 v211, s52, v224
	s_add_u32 s52, s43, 3
	s_and_b32 s52, s52, 7
	s_lshl_b32 s52, s52, 6
	s_nop 0
	v_add_u32_e32 v212, s52, v224
	s_add_u32 s52, s43, 4
	s_and_b32 s52, s52, 7
	s_lshl_b32 s52, s52, 6
	s_nop 0
	v_add_u32_e32 v213, s52, v224
	s_add_u32 s52, s43, 5
	s_and_b32 s52, s52, 7
	s_lshl_b32 s52, s52, 6
	s_nop 0
	v_add_u32_e32 v214, s52, v224
	s_add_u32 s52, s43, 6
	s_and_b32 s52, s52, 7
	s_lshl_b32 s52, s52, 6
	s_nop 0
	v_add_u32_e32 v215, s52, v224
	s_add_u32 s52, s43, 7
	s_and_b32 s52, s52, 7
	s_lshl_b32 s52, s52, 6
	s_nop 0
	v_add_u32_e32 v216, s52, v224
	v_and_b32_e32 v225, 8, v0
	v_cmp_eq_u32_e32 vcc, 0, v225
	v_mov_b32_e32 v225, 0xeeeeeeee
	s_nop 1
	v_cndmask_b32_e32 v210, v225, v196, vcc
	v_and_b32_e32 v225, 47, v0
	v_cmp_eq_u32_e64 s[4:5], 0, v225
	v_lshlrev_b32_e32 v225, 4, v167
	v_lshlrev_b32_e32 v226, 3, v201
	s_mov_b32 s52, 0x24400
	v_or3_b32 v218, v225, v226, s52
	s_load_dwordx2 s[6:7], s[0:1], 0x18
	s_lshl_b32 s11, s2, 9
	s_mov_b64 s[22:23], 0
	s_mov_b32 s29, 0
	s_mov_b32 s30, 0
	v_mov_b32_e32 v221, 0
	s_mov_b32 s40, 0x3a000000
	s_mov_b32 s41, 0x34800000
	s_mov_b32 s42, 0x45000000
	v_mov_b32_e32 v217, 0x24480
	v_mov_b64_e32 v[230:231], 0
	v_mov_b64_e32 v[232:233], 0
	v_mov_b64_e32 v[234:235], 0
	v_mov_b64_e32 v[236:237], 0
	v_mov_b64_e32 v[238:239], 0
	v_mov_b64_e32 v[240:241], 0
	v_mov_b64_e32 v[242:243], 0
	v_mov_b64_e32 v[244:245], 0
	ds_write_b128 v217, v[230:233]
	v_mov_b32_e32 v178, 0
	v_fma_mixlo_f16 v131, v178, v238, v171
	v_fma_mixlo_f16 v139, v178, v238, v170
	v_fma_mixlo_f16 v147, v178, v238, v169
	v_fma_mixlo_f16 v155, v178, v238, v168
	v_fma_f32 v130, v178, v238, v171
	v_fma_f32 v138, v178, v238, v170
	v_fma_f32 v146, v178, v238, v169
	v_fma_f32 v154, v178, v238, v168
	v_fma_mix_f32 v130, v130, 1.0, -v131 op_sel_hi:[0,0,1]
	v_fma_mix_f32 v138, v138, 1.0, -v139 op_sel_hi:[0,0,1]
	v_fma_mix_f32 v146, v146, 1.0, -v147 op_sel_hi:[0,0,1]
	v_fma_mix_f32 v154, v154, 1.0, -v155 op_sel_hi:[0,0,1]
	v_fma_mixlo_f16 v133, v130, s42, 0
	v_fma_mixlo_f16 v141, v138, s42, 0
	v_fma_mixlo_f16 v149, v146, s42, 0
	v_fma_mixlo_f16 v157, v154, s42, 0
	v_fma_mix_f32 v130, v130, s42, -v133 op_sel_hi:[0,0,1]
	v_fma_mix_f32 v138, v138, s42, -v141 op_sel_hi:[0,0,1]
	v_fma_mix_f32 v146, v146, s42, -v149 op_sel_hi:[0,0,1]
	v_fma_mix_f32 v154, v154, s42, -v157 op_sel_hi:[0,0,1]
	v_fma_mixlo_f16 v132, v130, s42, 0
	v_fma_mixlo_f16 v140, v138, s42, 0
	v_fma_mixlo_f16 v148, v146, s42, 0
	v_fma_mixlo_f16 v156, v154, s42, 0
	ds_write_b16 v204, v131
	ds_write_b16 v205, v139
	ds_write_b16 v206, v147
	ds_write_b16 v207, v155
	ds_write_b16 v204, v133 offset:544
	ds_write_b16 v205, v141 offset:544
	ds_write_b16 v206, v149 offset:544
	ds_write_b16 v207, v157 offset:544
	ds_write_b16 v204, v132 offset:1088
	ds_write_b16 v205, v140 offset:1088
	ds_write_b16 v206, v148 offset:1088
	ds_write_b16 v207, v156 offset:1088
	s_waitcnt lgkmcnt(0)
	s_barrier
	ds_read_b128 v[130:133], v208
	ds_read_b128 v[134:137], v209 offset:64
	ds_read_b128 v[138:141], v211
	ds_read_b128 v[142:145], v212
	ds_read_b128 v[146:149], v213
	ds_read_b128 v[150:153], v214
	ds_read_b128 v[154:157], v215
	ds_read_b128 v[158:161], v216
	ds_read_b128 v[180:183], v199 offset:0
	ds_read_b128 v[184:187], v199 offset:1024
	ds_read_b128 v[188:191], v199 offset:4096
	ds_read_b128 v[192:195], v199 offset:5120
	ds_read_b128 v[222:225], v199 offset:8192
	s_waitcnt lgkmcnt(6)
	ds_read_b128 v[226:229], v199 offset:9216
	v_smfmac_f32_16x16x64_f16 v[230:233], v[130:133], a[0:7], v210
	v_smfmac_f32_16x16x64_f16 v[234:237], v[130:133], v[18:25], v210
	v_smfmac_f32_16x16x64_f16 v[230:233], v[134:137], a[40:47], v210
	v_smfmac_f32_16x16x64_f16 v[234:237], v[134:137], v[34:41], v210
	v_smfmac_f32_16x16x64_f16 v[230:233], v[138:141], a[64:71], v210
	v_smfmac_f32_16x16x64_f16 v[234:237], v[138:141], v[42:49], v210
	v_smfmac_f32_16x16x64_f16 v[230:233], v[142:145], a[96:103], v210
	v_smfmac_f32_16x16x64_f16 v[234:237], v[142:145], v[58:65], v210
	v_smfmac_f32_16x16x64_f16 v[230:233], v[146:149], a[128:135], v210
	v_smfmac_f32_16x16x64_f16 v[234:237], v[146:149], v[74:81], v210
	v_smfmac_f32_16x16x64_f16 v[230:233], v[150:153], a[160:167], v210
	v_smfmac_f32_16x16x64_f16 v[234:237], v[150:153], v[98:105], v210
	v_smfmac_f32_16x16x64_f16 v[230:233], v[154:157], a[192:199], v210
	v_smfmac_f32_16x16x64_f16 v[234:237], v[154:157], v[106:113], v210
	s_waitcnt vmcnt(0)
	s_waitcnt lgkmcnt(6)
	v_smfmac_f32_16x16x64_f16 v[230:233], v[158:161], a[224:231], v210
	v_smfmac_f32_16x16x64_f16 v[234:237], v[158:161], v[122:129], v210
	v_smfmac_f32_16x16x64_f16 v[238:241], v[130:133], a[16:23], v210
	s_waitcnt lgkmcnt(4)
	v_smfmac_f32_16x16x64_f16 v[242:245], v[130:133], v[180:187], v210
	ds_read_b128 v[180:183], v199 offset:12288
	ds_read_b128 v[184:187], v199 offset:13312
	v_smfmac_f32_16x16x64_f16 v[238:241], v[134:137], a[48:55], v210
	v_fmac_f32_e32 v230, s40, v231
	s_waitcnt lgkmcnt(4)
	v_smfmac_f32_16x16x64_f16 v[242:245], v[134:137], v[188:195], v210
	ds_read_b128 v[188:191], v199 offset:16384
	ds_read_b128 v[192:195], v199 offset:17408
	v_fmac_f32_e32 v234, s40, v235
	v_smfmac_f32_16x16x64_f16 v[238:241], v[138:141], a[80:87], v210
	v_fmac_f32_e32 v230, s41, v232
	s_waitcnt lgkmcnt(4)
	v_smfmac_f32_16x16x64_f16 v[242:245], v[138:141], v[222:229], v210
	ds_read_b128 v[222:225], v199 offset:20480
	ds_read_b128 v[226:229], v199 offset:21504
	v_fmac_f32_e32 v234, s41, v236
	v_smfmac_f32_16x16x64_f16 v[238:241], v[142:145], a[112:119], v210
	s_nop 0
	v_permlane32_swap_b32_e32 v230, v234
	s_waitcnt lgkmcnt(4)
	v_smfmac_f32_16x16x64_f16 v[242:245], v[142:145], v[180:187], v210
	ds_read_b128 v[180:183], v199 offset:24576
	ds_read_b128 v[184:187], v199 offset:25600
	v_add_f32_e32 v173, v230, v234
	v_smfmac_f32_16x16x64_f16 v[238:241], v[146:149], a[144:151], v210
	ds_read_b128 v[230:233], v217
	s_waitcnt lgkmcnt(5)
	v_smfmac_f32_16x16x64_f16 v[242:245], v[146:149], v[188:195], v210
	ds_read_b128 v[188:191], v199 offset:28672
	ds_read_b128 v[192:195], v199 offset:29696
	ds_read_b128 v[234:237], v217
	v_smfmac_f32_16x16x64_f16 v[238:241], v[150:153], a[176:183], v210
	s_waitcnt lgkmcnt(6)
	v_smfmac_f32_16x16x64_f16 v[242:245], v[150:153], v[222:229], v210
	ds_read_b128 v[222:225], v199 offset:2048
	ds_read_b128 v[226:229], v199 offset:3072
	v_smfmac_f32_16x16x64_f16 v[238:241], v[154:157], a[208:215], v210
	s_waitcnt lgkmcnt(6)
	v_smfmac_f32_16x16x64_f16 v[242:245], v[154:157], v[180:187], v210
	ds_read_b128 v[180:183], v199 offset:6144
	ds_read_b128 v[184:187], v199 offset:7168
	v_smfmac_f32_16x16x64_f16 v[238:241], v[158:161], a[240:247], v210
	s_waitcnt lgkmcnt(5)
	v_smfmac_f32_16x16x64_f16 v[242:245], v[158:161], v[188:195], v210
	ds_read_b128 v[188:191], v199 offset:10240
	ds_read_b128 v[192:195], v199 offset:11264
	v_smfmac_f32_16x16x64_f16 v[230:233], v[130:133], a[8:15], v210
	s_waitcnt lgkmcnt(6)
	v_smfmac_f32_16x16x64_f16 v[234:237], v[130:133], v[2:9], v210
	v_smfmac_f32_16x16x64_f16 v[230:233], v[134:137], a[32:39], v210
	v_fmac_f32_e32 v238, s40, v239
	v_smfmac_f32_16x16x64_f16 v[234:237], v[134:137], v[10:17], v210
	v_fmac_f32_e32 v242, s40, v243
	v_smfmac_f32_16x16x64_f16 v[230:233], v[138:141], a[72:79], v210
	v_fmac_f32_e32 v238, s41, v240
	v_smfmac_f32_16x16x64_f16 v[234:237], v[138:141], v[50:57], v210
	v_fmac_f32_e32 v242, s41, v244
	v_smfmac_f32_16x16x64_f16 v[230:233], v[142:145], a[104:111], v210
	s_nop 0
	v_permlane32_swap_b32_e32 v238, v242
	v_smfmac_f32_16x16x64_f16 v[234:237], v[142:145], v[26:33], v210
	v_add_f32_e32 v175, v238, v242
	v_smfmac_f32_16x16x64_f16 v[230:233], v[146:149], a[136:143], v210
	ds_read_b128 v[238:241], v217
	v_smfmac_f32_16x16x64_f16 v[234:237], v[146:149], v[82:89], v210
	ds_read_b128 v[242:245], v217
	v_smfmac_f32_16x16x64_f16 v[230:233], v[150:153], a[168:175], v210
	v_smfmac_f32_16x16x64_f16 v[234:237], v[150:153], v[66:73], v210
	v_smfmac_f32_16x16x64_f16 v[230:233], v[154:157], a[200:207], v210
	v_smfmac_f32_16x16x64_f16 v[234:237], v[154:157], v[114:121], v210
	v_smfmac_f32_16x16x64_f16 v[230:233], v[158:161], a[232:239], v210
	v_smfmac_f32_16x16x64_f16 v[234:237], v[158:161], v[90:97], v210
	s_waitcnt lgkmcnt(1)
	v_smfmac_f32_16x16x64_f16 v[238:241], v[130:133], a[24:31], v210
	s_waitcnt lgkmcnt(0)
	v_smfmac_f32_16x16x64_f16 v[242:245], v[130:133], v[222:229], v210
	ds_read_b128 v[222:225], v199 offset:14336
	ds_read_b128 v[226:229], v199 offset:15360
	v_smfmac_f32_16x16x64_f16 v[238:241], v[134:137], a[56:63], v210
	v_fmac_f32_e32 v230, s40, v231
	v_smfmac_f32_16x16x64_f16 v[242:245], v[134:137], v[180:187], v210
	ds_read_b128 v[180:183], v199 offset:18432
	ds_read_b128 v[184:187], v199 offset:19456
	v_fmac_f32_e32 v234, s40, v235
	v_smfmac_f32_16x16x64_f16 v[238:241], v[138:141], a[88:95], v210
	v_fmac_f32_e32 v230, s41, v232
	v_smfmac_f32_16x16x64_f16 v[242:245], v[138:141], v[188:195], v210
	ds_read_b128 v[188:191], v199 offset:22528
	ds_read_b128 v[192:195], v199 offset:23552
	v_fmac_f32_e32 v234, s41, v236
	v_smfmac_f32_16x16x64_f16 v[238:241], v[142:145], a[120:127], v210
	s_nop 0
	v_permlane32_swap_b32_e32 v230, v234
	s_waitcnt lgkmcnt(4)
	v_smfmac_f32_16x16x64_f16 v[242:245], v[142:145], v[222:229], v210
	ds_read_b128 v[222:225], v199 offset:26624
	ds_read_b128 v[226:229], v199 offset:27648
	v_add_f32_e32 v172, v230, v234
	v_smfmac_f32_16x16x64_f16 v[238:241], v[146:149], a[152:159], v210
	ds_read_b128 v[230:233], v217
	s_waitcnt lgkmcnt(5)
	v_smfmac_f32_16x16x64_f16 v[242:245], v[146:149], v[180:187], v210
	ds_read_b128 v[180:183], v199 offset:30720
	ds_read_b128 v[184:187], v199 offset:31744
	ds_read_b128 v[234:237], v217
	v_smfmac_f32_16x16x64_f16 v[238:241], v[150:153], a[184:191], v210
	s_waitcnt lgkmcnt(6)
	v_smfmac_f32_16x16x64_f16 v[242:245], v[150:153], v[188:195], v210
	v_smfmac_f32_16x16x64_f16 v[238:241], v[154:157], a[216:223], v210
	s_waitcnt lgkmcnt(4)
	v_smfmac_f32_16x16x64_f16 v[242:245], v[154:157], v[222:229], v210
	v_smfmac_f32_16x16x64_f16 v[238:241], v[158:161], a[248:255], v210
	s_waitcnt lgkmcnt(1)
	v_smfmac_f32_16x16x64_f16 v[242:245], v[158:161], v[180:187], v210
	s_nop 5
	v_fmac_f32_e32 v238, s40, v239
	s_nop 0
	v_fmac_f32_e32 v242, s40, v243
	v_fmac_f32_e32 v238, s41, v240
	v_fmac_f32_e32 v242, s41, v244
	s_nop 1
	v_permlane32_swap_b32_e32 v238, v242
	v_add_f32_e32 v174, v238, v242
	s_mov_b32 s52, 0x3a83126f
	v_mov_b32_e32 v245, 0x358637bd
	v_fma_f32 v179, |v171|, s52, v245
	v_fma_f32 v196, |v170|, s52, v245
	v_fma_f32 v197, |v169|, s52, v245
	v_fma_f32 v198, |v168|, s52, v245
	v_rcp_f32_e32 v179, v179
	v_rcp_f32_e32 v196, v196
	v_rcp_f32_e32 v197, v197
	v_rcp_f32_e32 v198, v198
	v_mul_f32_e32 v238, v170, v196
	v_mul_f32_e32 v239, 0x3b000000, v172
	v_mul_f32_e32 v239, v239, v196
	v_mul_f32_e32 v130, v238, v238
	v_mul_f32_e32 v131, v239, v239
	v_mul_f32_e32 v238, v171, v179
	v_mul_f32_e32 v239, 0x3b000000, v173
	v_mul_f32_e32 v239, v239, v179
	v_fmac_f32_e32 v130, v238, v238
	v_fmac_f32_e32 v131, v239, v239
	v_mul_f32_e32 v238, v169, v197
	v_mul_f32_e32 v239, 0x3b000000, v175
	v_mul_f32_e32 v239, v239, v197
	v_fmac_f32_e32 v130, v238, v238
	v_fmac_f32_e32 v131, v239, v239
	v_mul_f32_e32 v238, v168, v198
	v_mul_f32_e32 v239, 0x3b000000, v174
	v_mul_f32_e32 v239, v239, v198
	v_fmac_f32_e32 v130, v238, v238
	v_fmac_f32_e32 v131, v239, v239
	s_nop 0
	v_add_f32_dpp v130, v130, v130 quad_perm:[1,0,3,2] row_mask:0xf bank_mask:0xf bound_ctrl:1
	v_add_f32_dpp v131, v131, v131 quad_perm:[1,0,3,2] row_mask:0xf bank_mask:0xf bound_ctrl:1
	s_nop 0
	v_add_f32_dpp v130, v130, v130 quad_perm:[2,3,0,1] row_mask:0xf bank_mask:0xf bound_ctrl:1
	v_add_f32_dpp v131, v131, v131 quad_perm:[2,3,0,1] row_mask:0xf bank_mask:0xf bound_ctrl:1
	s_nop 0
	v_add_f32_dpp v130, v130, v130 row_half_mirror row_mask:0xf bank_mask:0xf bound_ctrl:1
	v_add_f32_dpp v131, v131, v131 row_half_mirror row_mask:0xf bank_mask:0xf bound_ctrl:1
	s_nop 0
	v_add_f32_dpp v130, v130, v130 row_mirror row_mask:0xf bank_mask:0xf bound_ctrl:1
	v_add_f32_dpp v131, v131, v131 row_mirror row_mask:0xf bank_mask:0xf bound_ctrl:1
	v_mov_b32_e32 v240, v130
	v_mov_b32_e32 v241, v131
	s_nop 0
	v_permlane32_swap_b32_e32 v130, v240
	v_permlane32_swap_b32_e32 v131, v241
	v_add_f32_e32 v130, v130, v240
	v_add_f32_e32 v131, v131, v241
	v_add_u32_e32 v242, 0, v218
	v_lshlrev_b32_e32 v243, 3, v201
	v_or_b32_e32 v243, 0x24400, v243
	s_and_saveexec_b64 s[2:3], s[4:5]
	ds_write_b64 v242, v[130:131]
	s_or_b64 exec, exec, s[2:3]
	s_waitcnt lgkmcnt(0)
	s_barrier
	ds_read_b64 v[134:135], v243 offset:0
	ds_read_b64 v[138:139], v243 offset:16
	ds_read_b64 v[142:143], v243 offset:32
	ds_read_b64 v[146:147], v243 offset:48
	s_waitcnt lgkmcnt(2)
	v_add_f32_e32 v238, v134, v138
	s_waitcnt lgkmcnt(1)
	v_add_f32_e32 v238, v238, v142
	s_waitcnt lgkmcnt(0)
	v_add_f32_e32 v238, v238, v146
	v_add_f32_e32 v239, v135, v139
	v_add_f32_e32 v239, v239, v143
	v_add_f32_e32 v239, v239, v147
	v_mul_f32_e32 v238, 0x3b000000, v238
	v_max_f32_e32 v238, 0xda24260, v238
	v_sqrt_f32_e32 v238, v238
	v_mul_f32_e32 v239, 0x3b000000, v239
	v_max_f32_e32 v239, 0xda24260, v239
	v_sqrt_f32_e32 v239, v239
	s_nop 0
	v_mov_b32_e32 v220, v239
	v_rcp_f32_e32 v240, v239
	v_min_f32_e32 v241, v238, v239
	v_mul_f32_e32 v238, 0x3c23d70a, v238
	v_mul_f32_e32 v238, v238, v240
	s_mov_b32 s52, 0x3727c5ac
	v_cmp_ngt_f32_e32 vcc, s52, v241
	v_mov_b32_e32 v240, 0x358637bd
	s_nop 1
	v_cndmask_b32_e32 v219, v240, v238, vcc
	v_mul_f32_e32 v178, 0x3b000000, v219
	v_fma_mixlo_f16 v131, v178, v173, v171
	v_fma_mixlo_f16 v139, v178, v172, v170
	v_fma_mixlo_f16 v147, v178, v175, v169
	v_fma_mixlo_f16 v155, v178, v174, v168
	v_fma_f32 v130, v178, v173, v171
	v_fma_f32 v138, v178, v172, v170
	v_fma_f32 v146, v178, v175, v169
	v_fma_f32 v154, v178, v174, v168
	v_fma_mix_f32 v130, v130, 1.0, -v131 op_sel_hi:[0,0,1]
	v_fma_mix_f32 v138, v138, 1.0, -v139 op_sel_hi:[0,0,1]
	v_fma_mix_f32 v146, v146, 1.0, -v147 op_sel_hi:[0,0,1]
	v_fma_mix_f32 v154, v154, 1.0, -v155 op_sel_hi:[0,0,1]
	v_fma_mixlo_f16 v133, v130, s42, 0
	v_fma_mixlo_f16 v141, v138, s42, 0
	v_fma_mixlo_f16 v149, v146, s42, 0
	v_fma_mixlo_f16 v157, v154, s42, 0
	v_fma_mix_f32 v130, v130, s42, -v133 op_sel_hi:[0,0,1]
	v_fma_mix_f32 v138, v138, s42, -v141 op_sel_hi:[0,0,1]
	v_fma_mix_f32 v146, v146, s42, -v149 op_sel_hi:[0,0,1]
	v_fma_mix_f32 v154, v154, s42, -v157 op_sel_hi:[0,0,1]
	v_fma_mixlo_f16 v132, v130, s42, 0
	v_fma_mixlo_f16 v140, v138, s42, 0
	v_fma_mixlo_f16 v148, v146, s42, 0
	v_fma_mixlo_f16 v156, v154, s42, 0
	ds_write_b16 v204, v131 offset:8704
	ds_write_b16 v205, v139 offset:8704
	ds_write_b16 v206, v147 offset:8704
	ds_write_b16 v207, v155 offset:8704
	ds_write_b16 v204, v133 offset:9248
	ds_write_b16 v205, v141 offset:9248
	ds_write_b16 v206, v149 offset:9248
	ds_write_b16 v207, v157 offset:9248
	ds_write_b16 v204, v132 offset:9792
	ds_write_b16 v205, v140 offset:9792
	ds_write_b16 v206, v148 offset:9792
	ds_write_b16 v207, v156 offset:9792
	s_waitcnt lgkmcnt(0)
	s_barrier
	ds_read_b128 v[130:133], v208 offset:8704
	ds_read_b128 v[134:137], v209 offset:8768
	ds_read_b128 v[138:141], v211 offset:8704
	ds_read_b128 v[142:145], v212 offset:8704
	ds_read_b128 v[146:149], v213 offset:8704
	ds_read_b128 v[150:153], v214 offset:8704
	ds_read_b128 v[154:157], v215 offset:8704
	ds_read_b128 v[158:161], v216 offset:8704
	ds_read_b128 v[180:183], v199 offset:0
	ds_read_b128 v[184:187], v199 offset:1024
	ds_read_b128 v[188:191], v199 offset:4096
	ds_read_b128 v[192:195], v199 offset:5120
	ds_read_b128 v[222:225], v199 offset:8192
	s_waitcnt lgkmcnt(6)
	ds_read_b128 v[226:229], v199 offset:9216
	v_smfmac_f32_16x16x64_f16 v[230:233], v[130:133], a[0:7], v210
	ds_read_b128 v[238:241], v217
	v_smfmac_f32_16x16x64_f16 v[234:237], v[130:133], v[18:25], v210
	ds_read_b128 v[242:245], v217
	v_smfmac_f32_16x16x64_f16 v[230:233], v[134:137], a[40:47], v210
	v_smfmac_f32_16x16x64_f16 v[234:237], v[134:137], v[34:41], v210
	v_smfmac_f32_16x16x64_f16 v[230:233], v[138:141], a[64:71], v210
	v_smfmac_f32_16x16x64_f16 v[234:237], v[138:141], v[42:49], v210
	v_smfmac_f32_16x16x64_f16 v[230:233], v[142:145], a[96:103], v210
	v_smfmac_f32_16x16x64_f16 v[234:237], v[142:145], v[58:65], v210
	v_smfmac_f32_16x16x64_f16 v[230:233], v[146:149], a[128:135], v210
	v_smfmac_f32_16x16x64_f16 v[234:237], v[146:149], v[74:81], v210
	v_smfmac_f32_16x16x64_f16 v[230:233], v[150:153], a[160:167], v210
	v_smfmac_f32_16x16x64_f16 v[234:237], v[150:153], v[98:105], v210
	v_smfmac_f32_16x16x64_f16 v[230:233], v[154:157], a[192:199], v210
	v_smfmac_f32_16x16x64_f16 v[234:237], v[154:157], v[106:113], v210
	s_waitcnt lgkmcnt(8)
	v_smfmac_f32_16x16x64_f16 v[230:233], v[158:161], a[224:231], v210
	v_smfmac_f32_16x16x64_f16 v[234:237], v[158:161], v[122:129], v210
	s_waitcnt lgkmcnt(1)
	v_smfmac_f32_16x16x64_f16 v[238:241], v[130:133], a[16:23], v210
	s_waitcnt lgkmcnt(0)
	v_smfmac_f32_16x16x64_f16 v[242:245], v[130:133], v[180:187], v210
	ds_read_b128 v[180:183], v199 offset:12288
	ds_read_b128 v[184:187], v199 offset:13312
	v_smfmac_f32_16x16x64_f16 v[238:241], v[134:137], a[48:55], v210
	v_fmac_f32_e32 v230, s40, v231
	v_smfmac_f32_16x16x64_f16 v[242:245], v[134:137], v[188:195], v210
	ds_read_b128 v[188:191], v199 offset:16384
	ds_read_b128 v[192:195], v199 offset:17408
	v_fmac_f32_e32 v234, s40, v235
	v_smfmac_f32_16x16x64_f16 v[238:241], v[138:141], a[80:87], v210
	v_fmac_f32_e32 v230, s41, v232
	v_smfmac_f32_16x16x64_f16 v[242:245], v[138:141], v[222:229], v210
	ds_read_b128 v[222:225], v199 offset:20480
	ds_read_b128 v[226:229], v199 offset:21504
	v_fmac_f32_e32 v234, s41, v236
	v_smfmac_f32_16x16x64_f16 v[238:241], v[142:145], a[112:119], v210
	s_nop 0
	v_permlane32_swap_b32_e32 v230, v234
	s_waitcnt lgkmcnt(4)
	v_smfmac_f32_16x16x64_f16 v[242:245], v[142:145], v[180:187], v210
	ds_read_b128 v[180:183], v199 offset:24576
	ds_read_b128 v[184:187], v199 offset:25600
	v_add_f32_e32 v162, v230, v234
	v_smfmac_f32_16x16x64_f16 v[238:241], v[146:149], a[144:151], v210
	ds_read_b128 v[230:233], v217
	s_waitcnt lgkmcnt(5)
	v_smfmac_f32_16x16x64_f16 v[242:245], v[146:149], v[188:195], v210
	ds_read_b128 v[188:191], v199 offset:28672
	ds_read_b128 v[192:195], v199 offset:29696
	ds_read_b128 v[234:237], v217
	v_smfmac_f32_16x16x64_f16 v[238:241], v[150:153], a[176:183], v210
	s_waitcnt lgkmcnt(6)
	v_smfmac_f32_16x16x64_f16 v[242:245], v[150:153], v[222:229], v210
	ds_read_b128 v[222:225], v199 offset:2048
	ds_read_b128 v[226:229], v199 offset:3072
	v_smfmac_f32_16x16x64_f16 v[238:241], v[154:157], a[208:215], v210
	s_waitcnt lgkmcnt(6)
	v_smfmac_f32_16x16x64_f16 v[242:245], v[154:157], v[180:187], v210
	ds_read_b128 v[180:183], v199 offset:6144
	ds_read_b128 v[184:187], v199 offset:7168
	v_smfmac_f32_16x16x64_f16 v[238:241], v[158:161], a[240:247], v210
	s_waitcnt lgkmcnt(5)
	v_smfmac_f32_16x16x64_f16 v[242:245], v[158:161], v[188:195], v210
	ds_read_b128 v[188:191], v199 offset:10240
	ds_read_b128 v[192:195], v199 offset:11264
	v_smfmac_f32_16x16x64_f16 v[230:233], v[130:133], a[8:15], v210
	s_waitcnt lgkmcnt(6)
	v_smfmac_f32_16x16x64_f16 v[234:237], v[130:133], v[2:9], v210
	v_smfmac_f32_16x16x64_f16 v[230:233], v[134:137], a[32:39], v210
	v_fmac_f32_e32 v238, s40, v239
	v_smfmac_f32_16x16x64_f16 v[234:237], v[134:137], v[10:17], v210
	v_fmac_f32_e32 v242, s40, v243
	v_smfmac_f32_16x16x64_f16 v[230:233], v[138:141], a[72:79], v210
	v_fmac_f32_e32 v238, s41, v240
	v_smfmac_f32_16x16x64_f16 v[234:237], v[138:141], v[50:57], v210
	v_fmac_f32_e32 v242, s41, v244
	v_smfmac_f32_16x16x64_f16 v[230:233], v[142:145], a[104:111], v210
	s_nop 0
	v_permlane32_swap_b32_e32 v238, v242
	v_smfmac_f32_16x16x64_f16 v[234:237], v[142:145], v[26:33], v210
	v_add_f32_e32 v164, v238, v242
	v_smfmac_f32_16x16x64_f16 v[230:233], v[146:149], a[136:143], v210
	ds_read_b128 v[238:241], v217
	v_smfmac_f32_16x16x64_f16 v[234:237], v[146:149], v[82:89], v210
	ds_read_b128 v[242:245], v217
	v_smfmac_f32_16x16x64_f16 v[230:233], v[150:153], a[168:175], v210
	v_smfmac_f32_16x16x64_f16 v[234:237], v[150:153], v[66:73], v210
	v_smfmac_f32_16x16x64_f16 v[230:233], v[154:157], a[200:207], v210
	v_smfmac_f32_16x16x64_f16 v[234:237], v[154:157], v[114:121], v210
	v_smfmac_f32_16x16x64_f16 v[230:233], v[158:161], a[232:239], v210
	v_smfmac_f32_16x16x64_f16 v[234:237], v[158:161], v[90:97], v210
	s_waitcnt lgkmcnt(1)
	v_smfmac_f32_16x16x64_f16 v[238:241], v[130:133], a[24:31], v210
	s_waitcnt lgkmcnt(0)
	v_smfmac_f32_16x16x64_f16 v[242:245], v[130:133], v[222:229], v210
	ds_read_b128 v[222:225], v199 offset:14336
	ds_read_b128 v[226:229], v199 offset:15360
	v_smfmac_f32_16x16x64_f16 v[238:241], v[134:137], a[56:63], v210
	v_fmac_f32_e32 v230, s40, v231
	v_smfmac_f32_16x16x64_f16 v[242:245], v[134:137], v[180:187], v210
	ds_read_b128 v[180:183], v199 offset:18432
	ds_read_b128 v[184:187], v199 offset:19456
	v_fmac_f32_e32 v234, s40, v235
	v_smfmac_f32_16x16x64_f16 v[238:241], v[138:141], a[88:95], v210
	v_fmac_f32_e32 v230, s41, v232
	v_smfmac_f32_16x16x64_f16 v[242:245], v[138:141], v[188:195], v210
	ds_read_b128 v[188:191], v199 offset:22528
	ds_read_b128 v[192:195], v199 offset:23552
	v_fmac_f32_e32 v234, s41, v236
	v_smfmac_f32_16x16x64_f16 v[238:241], v[142:145], a[120:127], v210
	s_nop 0
	v_permlane32_swap_b32_e32 v230, v234
	s_waitcnt lgkmcnt(4)
	v_smfmac_f32_16x16x64_f16 v[242:245], v[142:145], v[222:229], v210
	ds_read_b128 v[222:225], v199 offset:26624
	ds_read_b128 v[226:229], v199 offset:27648
	v_add_f32_e32 v163, v230, v234
	v_smfmac_f32_16x16x64_f16 v[238:241], v[146:149], a[152:159], v210
	ds_read_b128 v[230:233], v217
	s_waitcnt lgkmcnt(5)
	v_smfmac_f32_16x16x64_f16 v[242:245], v[146:149], v[180:187], v210
	ds_read_b128 v[180:183], v199 offset:30720
	ds_read_b128 v[184:187], v199 offset:31744
	ds_read_b128 v[234:237], v217
	v_smfmac_f32_16x16x64_f16 v[238:241], v[150:153], a[184:191], v210
	s_waitcnt lgkmcnt(6)
	v_smfmac_f32_16x16x64_f16 v[242:245], v[150:153], v[188:195], v210
	v_smfmac_f32_16x16x64_f16 v[238:241], v[154:157], a[216:223], v210
	s_waitcnt lgkmcnt(4)
	v_smfmac_f32_16x16x64_f16 v[242:245], v[154:157], v[222:229], v210
	v_smfmac_f32_16x16x64_f16 v[238:241], v[158:161], a[248:255], v210
	s_waitcnt lgkmcnt(1)
	v_smfmac_f32_16x16x64_f16 v[242:245], v[158:161], v[180:187], v210
	s_nop 5
	v_fmac_f32_e32 v238, s40, v239
	s_nop 0
	v_fmac_f32_e32 v242, s40, v243
	v_fmac_f32_e32 v238, s41, v240
	v_fmac_f32_e32 v242, s41, v244
	s_nop 1
	v_permlane32_swap_b32_e32 v238, v242
	v_add_f32_e32 v165, v238, v242
	v_sub_f32_e32 v238, v163, v172
	v_mul_f32_e32 v238, 0x3b000000, v238
	v_mul_f32_e32 v238, v238, v196
	v_mul_f32_e32 v130, v238, v238
	v_sub_f32_e32 v238, v162, v173
	v_mul_f32_e32 v238, 0x3b000000, v238
	v_mul_f32_e32 v238, v238, v179
	v_fmac_f32_e32 v130, v238, v238
	v_sub_f32_e32 v238, v164, v175
	v_mul_f32_e32 v238, 0x3b000000, v238
	v_mul_f32_e32 v238, v238, v197
	v_fmac_f32_e32 v130, v238, v238
	v_sub_f32_e32 v238, v165, v174
	v_mul_f32_e32 v238, 0x3b000000, v238
	v_mul_f32_e32 v238, v238, v198
	v_fmac_f32_e32 v130, v238, v238
	s_nop 1
	v_add_f32_dpp v130, v130, v130 quad_perm:[1,0,3,2] row_mask:0xf bank_mask:0xf bound_ctrl:1
	s_nop 1
	v_add_f32_dpp v130, v130, v130 quad_perm:[2,3,0,1] row_mask:0xf bank_mask:0xf bound_ctrl:1
	s_nop 1
	v_add_f32_dpp v130, v130, v130 row_half_mirror row_mask:0xf bank_mask:0xf bound_ctrl:1
	s_nop 1
	v_add_f32_dpp v130, v130, v130 row_mirror row_mask:0xf bank_mask:0xf bound_ctrl:1
	v_mov_b32_e32 v240, v130
	s_nop 1
	v_permlane32_swap_b32_e32 v130, v240
	v_add_f32_e32 v130, v130, v240
	v_add_u32_e32 v242, 64, v218
	v_lshlrev_b32_e32 v243, 3, v201
	v_or_b32_e32 v243, 0x24440, v243
	s_and_saveexec_b64 s[2:3], s[4:5]
	ds_write_b32 v242, v130
	s_or_b64 exec, exec, s[2:3]
	s_waitcnt lgkmcnt(0)
	s_barrier
	ds_read2_b32 v[134:135], v243 offset1:4
	ds_read2_b32 v[136:137], v243 offset0:8 offset1:12
	s_waitcnt lgkmcnt(1)
	v_add_f32_e32 v238, v134, v135
	s_waitcnt lgkmcnt(0)
	v_add_f32_e32 v238, v238, v136
	v_add_f32_e32 v238, v238, v137
	v_mul_f32_e32 v238, 0x3b000000, v238
	v_max_f32_e32 v238, 0xda24260, v238
	v_rcp_f32_e32 v240, v219
	v_sqrt_f32_e32 v238, v238
	s_nop 0
	v_mul_f32_e32 v238, v240, v238
	v_max_f32_e32 v241, v220, v238
	v_mul_f32_e32 v242, 0x3a83126f, v219
	v_max_f32_e32 v242, 0x358637bd, v242
	v_max_f32_e32 v243, 0x26901d7d, v241
	v_rcp_f32_e32 v243, v243
	s_nop 0
	v_mul_f32_e32 v243, 0x3c23d70a, v243
	v_log_f32_e32 v243, v243
	s_nop 0
	v_mul_f32_e32 v243, 0x3e4ccccd, v243
	v_exp_f32_e32 v243, v243
	s_mov_b32 s52, 0x26901d7d
	v_cmp_ge_f32_e32 vcc, s52, v241
	s_nop 1
	v_cndmask_b32_e32 v243, v243, v242, vcc
	v_mul_f32_e32 v242, 0x42c80000, v219
	v_min3_f32 v1, v242, v243, 1.0
